# moe_gu/moe_dn unit heads read the tile count NTt from a spare VGPR lane (written once in the phase preamble) instead of an LDS round trip per unit (on top of v55)
# speedup vs baseline: 1.0070x; 1.0070x over previous
.LBB0_1529:
	s_or_b64 exec, exec, s[4:5]
	v_readfirstlane_b32 s0, v188
	s_ashr_i32 s6, s0, 6
	s_lshl_b32 s1, s6, 5
	v_lshrrev_b32_e32 v1, 4, v188
	s_and_b32 s1, s1, 0x60
	s_ashr_i32 s12, s0, 8
	v_and_b32_e32 v0, 15, v188
	v_bfe_u32 v2, v1, 1, 1
	v_lshlrev_b32_e32 v1, 1, v188
	v_lshlrev_b32_e32 v5, 2, v188
	s_lshr_b32 s3, s1, 3
	v_and_b32_e32 v3, 32, v1
	s_lshl_b32 s2, s12, 13
	v_lshlrev_b32_e32 v4, 10, v2
	v_lshlrev_b32_e32 v1, 6, v0
	v_and_b32_e32 v5, 32, v5
	v_or_b32_e32 v2, s3, v2
	v_writelane_b32 v255, s0, 36
	v_bitop3_b32 v3, v1, v5, v3 bitop3:0x36
	v_lshlrev_b32_e32 v2, 10, v2
	s_add_i32 s2, s2, 0
	v_readlane_b32 s0, v254, 41
	v_and_b32_e32 v5, 16, v188
	v_add3_u32 v4, s2, v3, v4
	v_add3_u32 v2, s0, v3, v2
	v_bitop3_b32 v3, v188, 16, v188 bitop3:0xc
	v_readlane_b32 s0, v254, 53
	v_mov_b32_e32 v189, 0x7f7f7f7f
	v_add_u32_e32 v190, v5, v4
	v_add_u32_e32 v191, v5, v2
	v_add_u32_e32 v192, v3, v4
	v_add_u32_e32 v193, v3, v2
	v_mov_b32_e32 v2, s0
	s_waitcnt lgkmcnt(0)
	s_barrier
	ds_read_b32 v2, v2
	v_readlane_b32 s2, v253, 56
	v_readlane_b32 s3, v253, 57
	s_and_b64 vcc, exec, s[2:3]
	s_waitcnt lgkmcnt(0)
	v_readfirstlane_b32 s7, v2
	s_nop 1
	v_writelane_b32 v255, s7, 43
	s_cbranch_vccz .LBB0_1531
	s_lshl_b32 s4, s7, 3
	s_cmp_lt_i32 s94, s4
	s_mov_b64 s[2:3], 0
	s_cselect_b64 s[4:5], -1, 0
	s_branch .LBB0_1532

.LBB0_1541:
	v_readlane_b32 s0, v254, 53
	v_readlane_b32 s2, v253, 56
	v_readlane_b32 s3, v253, 57
	s_add_i32 s1, s57, 1
	s_and_b64 vcc, exec, s[2:3]
	s_waitcnt lgkmcnt(0)
	v_readlane_b32 s3, v255, 43
	s_cbranch_vccz .LBB0_1560
	s_mul_i32 s15, s1, s37
	s_add_i32 s15, s15, s94
	s_lshl_b32 s2, s3, 3
	s_mov_b64 s[18:19], 0
	s_cmp_lt_i32 s15, s2
	s_mov_b64 s[16:17], 0
	s_cbranch_scc0 .LBB0_1544
	s_ashr_i32 s2, s15, 31
	s_lshr_b32 s2, s2, 29
	s_add_i32 s14, s15, s2
	s_ashr_i32 s2, s14, 3
	s_and_b32 s14, s14, -8
	s_sub_i32 s14, s15, s14
	s_mov_b64 s[16:17], -1
	s_and_b64 vcc, exec, s[18:19]
	s_cbranch_vccz .LBB0_1561
	s_branch .LBB0_1545

.LBB0_1621:
	v_mbcnt_lo_u32_b32 v0, -1, 0
	v_mbcnt_hi_u32_b32 v0, -1, v0
	v_lshl_add_u32 v160, s43, 6, v0
	s_nop 0
	v_readfirstlane_b32 s28, v160
	s_ashr_i32 s6, s28, 6
	s_lshl_b32 s3, s6, 5
	v_lshrrev_b32_e32 v1, 4, v160
	v_bfe_u32 v2, v160, 4, 2
	s_and_b32 s8, s3, 0x60
	s_ashr_i32 s9, s28, 8
	v_and_b32_e32 v0, 15, v160
	v_bfe_u32 v4, v1, 1, 1
	v_lshlrev_b32_e32 v1, 5, v2
	v_lshlrev_b32_e32 v7, 2, v160
	s_lshr_b32 s3, s8, 3
	v_and_b32_e32 v5, 32, v1
	s_lshl_b32 s2, s9, 13
	v_lshlrev_b32_e32 v6, 10, v4
	v_lshlrev_b32_e32 v3, 6, v0
	v_and_b32_e32 v7, 32, v7
	v_or_b32_e32 v4, s3, v4
	v_bitop3_b32 v5, v3, v7, v5 bitop3:0x36
	v_lshlrev_b32_e32 v4, 10, v4
	s_add_i32 s2, s2, 0
	v_readlane_b32 s0, v254, 41
	v_and_b32_e32 v7, 16, v160
	v_add3_u32 v6, s2, v5, v6
	v_add3_u32 v4, s0, v5, v4
	v_bitop3_b32 v5, v160, 16, v160 bitop3:0xc
	v_readlane_b32 s0, v254, 53
	v_mov_b32_e32 v188, 0x7f7f7f7f
	v_add_u32_e32 v189, v7, v6
	v_add_u32_e32 v190, v7, v4
	v_add_u32_e32 v191, v5, v6
	v_add_u32_e32 v192, v5, v4
	v_mov_b32_e32 v4, s0
	s_waitcnt lgkmcnt(0)
	s_barrier
	ds_read_b32 v4, v4
	v_readlane_b32 s2, v253, 62
	v_readlane_b32 s3, v253, 63
	s_and_b64 vcc, exec, s[2:3]
	s_waitcnt lgkmcnt(0)
	v_readfirstlane_b32 s7, v4
	s_nop 1
	v_writelane_b32 v255, s7, 43
	s_cbranch_vccz .LBB0_1646
	s_lshl_b32 s4, s7, 2
	s_cmp_lt_i32 s94, s4
	s_mov_b64 s[2:3], 0
	s_cselect_b64 s[4:5], -1, 0
	s_branch .LBB0_1647

.LBB0_1656:
	v_readlane_b32 s0, v254, 53
	v_readlane_b32 s16, v253, 62
	v_readlane_b32 s17, v253, 63
	s_add_i32 s73, s82, 1
	s_and_b64 vcc, exec, s[16:17]
	s_waitcnt lgkmcnt(0)
	v_readlane_b32 s7, v255, 43
	s_cbranch_vccz .LBB0_1669
	s_mul_i32 s17, s73, s37
	s_add_i32 s17, s17, s94
	s_lshl_b32 s16, s7, 2
	s_mov_b64 s[26:27], 0
	s_cmp_lt_i32 s17, s16
	s_mov_b64 s[20:21], 0
	s_cbranch_scc0 .LBB0_1659
	s_ashr_i32 s16, s17, 31
	s_lshr_b32 s16, s16, 30
	s_add_i32 s18, s17, s16
	s_ashr_i32 s16, s18, 2
	s_and_b32 s18, s18, -4
	s_sub_i32 s18, s17, s18
	s_mov_b64 s[20:21], -1
	s_and_b64 vcc, exec, s[26:27]
	s_cbranch_vccz .LBB0_1670
	s_branch .LBB0_1660
